# phases B and D: bit 10 of the wave index flipped for the per-wave transpose unit loops, so their extra units land on workgroups that run one GLA iteration fewer
# baseline (speedup 1.0000x reference)
; #define LAS __attribute__((address_space(3)))
; __device__ __forceinline__ void ph_transposes(Frame& F, int l) {
;     LAS bf16_t* tile = (LAS bf16_t*)(F.lds + F.wave * 16384);
;     const bf16_t* U = (const bf16_t*)(F.ws + WS_U);
;     const int gw = F.wg * NWAVES + F.wave, NGW = F.G * NWAVES;
;     const int rsub = F.lane >> 3, cseg = F.lane & 7;
;     for (int u = gw; u < 1088 * 12; u += NGW) {
;         const int tt = u / 12, blk = u % 12;
;         int b, s0, Ls, rowbase, posbase;
;         if (tt < 1024) { b = tt >> 6; s0 = (tt & 63) * 64; Ls = SEQ; rowbase = b * SEQ; posbase = 0; }
;         else { const int t2 = tt - 1024; b = t2 >> 2; s0 = (t2 & 3) * 64; Ls = CTXL; rowbase = NLAT + b * CTXL; posbase = SEQ; }
;         if (blk < 12) {
.LBB0_383:
	s_andn2_b64 vcc, exec, s[2:3]
	s_cbranch_vccnz .LBB0_469
	v_readlane_b32 s36, v252, 8
	v_readlane_b32 s37, v252, 9
	v_readlane_b32 s38, v252, 10
	v_readlane_b32 s39, v252, 11
	s_mov_b32 s0, s97
	s_mov_b64 s[2:3], s[38:39]
	s_mov_b64 s[4:5], s[36:37]
	v_mbcnt_lo_u32_b32 v0, -1, 0
	v_mbcnt_hi_u32_b32 v0, -1, v0
	s_nop 0
	v_readlane_b32 s4, v254, 28
	s_add_i32 s52, s0, s4
	s_xor_b32 s52, s52, 0x400
	s_cmpk_gt_i32 s52, 0x32ff
	s_cbranch_scc1 .LBB0_398
	s_add_u32 s38, s2, 0x1b300000
	s_mul_i32 s4, s30, 0x900
	v_lshlrev_b32_e32 v1, 3, v0
	s_addc_u32 s39, s3, 0
	v_ashrrev_i32_e32 v37, 3, v0
	s_lshl_b32 s0, s0, 14
	s_add_i32 s40, s4, 0x300
	v_and_b32_e32 v36, 56, v1
	s_movk_i32 s4, 0xa0
	s_add_i32 s0, s0, 0
	v_mul_lo_u32 v2, v37, s4
	v_lshlrev_b32_e32 v3, 1, v36
	v_cmp_gt_i32_e32 vcc, 8, v0
	v_mov_b32_e32 v1, s0
	v_add3_u32 v43, s0, v2, v3
	v_cmp_gt_i32_e64 s[36:37], 16, v0
	s_waitcnt vmcnt(0)
	v_cndmask_b32_e64 v59, 64, -1, vcc
	v_cmp_lt_i32_e32 vcc, 7, v0
	v_mov_b32_e32 v0, 0x90
	s_add_u32 s42, s2, 0x43900000
	v_readlane_b32 s0, v255, 24
	v_mad_u32_u24 v1, v36, s4, v1
	v_cndmask_b32_e32 v0, 14, v0, vcc
	s_addc_u32 s43, s3, 0
	v_readlane_b32 s2, v255, 14
	v_add_u32_e32 v63, s0, v37
	v_readlane_b32 s0, v255, 23
	v_lshl_add_u32 v41, v37, 1, v1
	v_add_u32_e32 v45, 0x500, v43
	v_add_u32_e32 v47, 0xa00, v43
	v_add_u32_e32 v49, 0xf00, v43
	v_add_u32_e32 v51, 0x1400, v43
	v_add_u32_e32 v53, 0x1900, v43
	v_add_u32_e32 v55, 0x1e00, v43
	v_add_u32_e32 v57, 0x2300, v43
	v_add_u32_e32 v61, v1, v0
	s_ashr_i32 s41, s40, 31
	s_lshl_b32 s53, s52, 6
	s_lshl_b32 s54, s2, 6
	v_add_u32_e32 v65, s0, v37
	v_readlane_b32 s3, v255, 15
	s_branch .LBB0_387

; #define LAS __attribute__((address_space(3)))
; __device__ __forceinline__ void ph_hy_transpose(Frame& F, bool last) {
;     LAS bf16_t* tile = (LAS bf16_t*)(F.lds + F.wave * 16384);
;     const bf16_t* HYO = (const bf16_t*)(F.ws + WS_Y);
;     const int gw = F.wg * NWAVES + F.wave, NGW = F.G * NWAVES;
;     const int rsub = F.lane >> 3, cseg = F.lane & 7;
;     const int ntt = last ? 1024 : 1088;
;     for (int u = gw; u < ntt * 4; u += NGW) {
;         const int tt = u >> 2, cb = u & 3;
;         int b, s0, rowbase, posbase;
;         if (tt < 1024) { b = tt >> 6; s0 = (tt & 63) * 64; rowbase = b * SEQ; posbase = 0; }
;         else { const int t2 = tt - 1024; b = t2 >> 2; s0 = (t2 & 3) * 64; rowbase = NLAT + b * CTXL; posbase = SEQ; }
.LBB0_602:
	s_andn2_b64 vcc, exec, s[2:3]
	s_cbranch_vccnz .LBB0_685
	v_readlane_b32 s36, v252, 8
	v_readlane_b32 s37, v252, 9
	v_readlane_b32 s38, v252, 10
	v_readlane_b32 s39, v252, 11
	s_mov_b32 s0, s97
	s_mov_b64 s[2:3], s[38:39]
	s_mov_b64 s[4:5], s[36:37]
	v_mbcnt_lo_u32_b32 v0, -1, 0
	v_mbcnt_hi_u32_b32 v0, -1, v0
	v_readlane_b32 s8, v255, 30
	v_readlane_b32 s4, v254, 28
	s_add_i32 s4, s0, s4
	s_xor_b32 s4, s4, 0x400
	v_readlane_b32 s9, v255, 31
	s_and_b64 s[18:19], s[8:9], exec
	s_movk_i32 s5, 0x1100
	s_cselect_b32 s20, 0x1000, s5
	s_cmp_ge_i32 s4, s20
	s_cbranch_scc1 .LBB0_614
	s_lshl_b32 s5, s0, 6
	v_ashrrev_i32_e32 v8, 3, v0
	s_and_b32 s5, s5, 0xc0
	v_lshlrev_b32_e32 v1, 3, v0
	s_waitcnt vmcnt(0)
	v_add_u32_e32 v6, s5, v8
	s_lshl_b32 s0, s0, 14
	v_and_b32_e32 v4, 56, v1
	v_add_u32_e32 v1, 8, v6
	v_lshlrev_b32_e32 v0, 4, v0
	s_add_u32 s18, s2, 0x52900000
	v_mad_i64_i32 v[2:3], s[36:37], v1, s15, 0
	v_and_b32_e32 v7, 0x70, v0
	v_mul_u32_u24_e32 v5, 0x90, v4
	s_addc_u32 s19, s3, 0
	v_or_b32_e32 v2, v2, v7
	v_lshl_add_u64 v[0:1], s[18:19], 0, v[2:3]
	v_or_b32_e32 v2, s0, v5
	v_lshlrev_b32_e32 v3, 1, v8
	s_waitcnt lgkmcnt(0)
	v_add3_u32 v9, v2, v3, 0
	v_mad_i64_i32 v[2:3], s[36:37], v6, s15, 0
	v_mul_lo_u32 v5, v8, s6
	v_or_b32_e32 v2, v2, v7
	v_add_u32_e32 v5, s0, v5
	v_lshl_add_u64 v[2:3], s[18:19], 0, v[2:3]
	v_add3_u32 v10, v5, v7, 0
	s_lshl_b32 s22, s5, 1
	v_lshlrev_b32_e32 v192, 1, v4
